# adds: expert-slot assignment scans the task's 128 selections from registers (two LDS batches) instead of one LDS round trip per entry
# baseline (speedup 1.0000x reference)
.LBB0_1290:
	s_or_b64 exec, exec, s[82:83]
	s_waitcnt lgkmcnt(0)
	s_barrier
	s_and_saveexec_b64 s[4:5], s[6:7]
	s_cbranch_execz .LBB0_1283
	ds_read_b128 v[2:5], v67 offset:41984
	ds_read_b128 v[6:9], v67 offset:42000
	ds_read_b128 v[10:13], v67 offset:42016
	ds_read_b128 v[14:17], v67 offset:42032
	s_waitcnt lgkmcnt(3)
	v_cmp_eq_u32_e32 vcc, v3, v0
	s_nop 1
	v_cndmask_b32_e64 v3, 0, 1, vcc
	v_cmp_eq_u32_e32 vcc, v2, v0
	s_nop 1
	v_addc_co_u32_e32 v2, vcc, 0, v3, vcc
	v_cmp_eq_u32_e32 vcc, v4, v0
	s_nop 1
	v_cndmask_b32_e64 v3, 0, 1, vcc
	v_cmp_eq_u32_e32 vcc, v5, v0
	s_nop 1
	v_addc_co_u32_e32 v2, vcc, v2, v3, vcc
	s_waitcnt lgkmcnt(2)
	v_cmp_eq_u32_e32 vcc, v6, v0
	s_nop 1
	v_cndmask_b32_e64 v3, 0, 1, vcc
	v_cmp_eq_u32_e32 vcc, v7, v0
	s_nop 1
	v_addc_co_u32_e32 v2, vcc, v2, v3, vcc
	v_cmp_eq_u32_e32 vcc, v8, v0
	s_nop 1
	v_cndmask_b32_e64 v3, 0, 1, vcc
	v_cmp_eq_u32_e32 vcc, v9, v0
	s_nop 1
	v_addc_co_u32_e32 v2, vcc, v2, v3, vcc
	s_waitcnt lgkmcnt(1)
	v_cmp_eq_u32_e32 vcc, v10, v0
	s_nop 1
	v_cndmask_b32_e64 v3, 0, 1, vcc
	v_cmp_eq_u32_e32 vcc, v11, v0
	s_nop 1
	v_addc_co_u32_e32 v2, vcc, v2, v3, vcc
	v_cmp_eq_u32_e32 vcc, v12, v0
	s_nop 1
	v_cndmask_b32_e64 v3, 0, 1, vcc
	v_cmp_eq_u32_e32 vcc, v13, v0
	s_nop 1
	v_addc_co_u32_e32 v2, vcc, v2, v3, vcc
	s_waitcnt lgkmcnt(0)
	v_cmp_eq_u32_e32 vcc, v14, v0
	s_nop 1
	v_cndmask_b32_e64 v3, 0, 1, vcc
	v_cmp_eq_u32_e32 vcc, v15, v0
	s_nop 1
	v_addc_co_u32_e32 v6, vcc, v2, v3, vcc
	ds_read_b128 v[2:5], v67 offset:42048
	v_cmp_eq_u32_e32 vcc, v16, v0
	s_nop 1
	v_cndmask_b32_e64 v7, 0, 1, vcc
	v_cmp_eq_u32_e32 vcc, v17, v0
	s_nop 1
	v_addc_co_u32_e32 v10, vcc, v6, v7, vcc
	ds_read_b128 v[6:9], v67 offset:42064
	s_waitcnt lgkmcnt(1)
	v_cmp_eq_u32_e32 vcc, v2, v0
	s_nop 1
	v_cndmask_b32_e64 v2, 0, 1, vcc
	v_cmp_eq_u32_e32 vcc, v3, v0
	s_nop 1
	v_addc_co_u32_e32 v2, vcc, v10, v2, vcc
	v_cmp_eq_u32_e32 vcc, v4, v0
	s_nop 1
	v_cndmask_b32_e64 v3, 0, 1, vcc
	v_cmp_eq_u32_e32 vcc, v5, v0
	s_nop 1
	v_addc_co_u32_e32 v2, vcc, v2, v3, vcc
	s_waitcnt lgkmcnt(0)
	v_cmp_eq_u32_e32 vcc, v6, v0
	s_nop 1
	v_cndmask_b32_e64 v3, 0, 1, vcc
	v_cmp_eq_u32_e32 vcc, v7, v0
	s_nop 1
	v_addc_co_u32_e32 v6, vcc, v2, v3, vcc
	ds_read_b128 v[2:5], v67 offset:42080
	v_cmp_eq_u32_e32 vcc, v8, v0
	s_nop 1
	v_cndmask_b32_e64 v7, 0, 1, vcc
	v_cmp_eq_u32_e32 vcc, v9, v0
	s_nop 1
	v_addc_co_u32_e32 v10, vcc, v6, v7, vcc
	ds_read_b128 v[6:9], v67 offset:42096
	s_waitcnt lgkmcnt(1)
	v_cmp_eq_u32_e32 vcc, v2, v0
	s_nop 1
	v_cndmask_b32_e64 v2, 0, 1, vcc
	v_cmp_eq_u32_e32 vcc, v3, v0
	s_nop 1
	v_addc_co_u32_e32 v2, vcc, v10, v2, vcc
	v_cmp_eq_u32_e32 vcc, v4, v0
	s_nop 1
	v_cndmask_b32_e64 v3, 0, 1, vcc
	v_cmp_eq_u32_e32 vcc, v5, v0
	s_nop 1
	v_addc_co_u32_e32 v2, vcc, v2, v3, vcc
	s_waitcnt lgkmcnt(0)
	v_cmp_eq_u32_e32 vcc, v6, v0
	s_nop 1
	v_cndmask_b32_e64 v3, 0, 1, vcc
	v_cmp_eq_u32_e32 vcc, v7, v0
	s_nop 1
	v_addc_co_u32_e32 v6, vcc, v2, v3, vcc
	ds_read_b128 v[2:5], v67 offset:42112
	v_cmp_eq_u32_e32 vcc, v8, v0
	s_nop 1
	v_cndmask_b32_e64 v7, 0, 1, vcc
	v_cmp_eq_u32_e32 vcc, v9, v0
	s_nop 1
	v_addc_co_u32_e32 v10, vcc, v6, v7, vcc
	ds_read_b128 v[6:9], v67 offset:42128
	s_waitcnt lgkmcnt(1)
	v_cmp_eq_u32_e32 vcc, v2, v0
	s_nop 1
	v_cndmask_b32_e64 v2, 0, 1, vcc
	v_cmp_eq_u32_e32 vcc, v3, v0
	s_nop 1
	v_addc_co_u32_e32 v2, vcc, v10, v2, vcc
	v_cmp_eq_u32_e32 vcc, v4, v0
	s_nop 1
	v_cndmask_b32_e64 v3, 0, 1, vcc
	v_cmp_eq_u32_e32 vcc, v5, v0
	s_nop 1
	v_addc_co_u32_e32 v2, vcc, v2, v3, vcc
	s_waitcnt lgkmcnt(0)
	v_cmp_eq_u32_e32 vcc, v6, v0
	s_nop 1
	v_cndmask_b32_e64 v3, 0, 1, vcc
	v_cmp_eq_u32_e32 vcc, v7, v0
	s_nop 1
	v_addc_co_u32_e32 v6, vcc, v2, v3, vcc
	ds_read_b128 v[2:5], v67 offset:42144
	v_cmp_eq_u32_e32 vcc, v8, v0
	s_nop 1
	v_cndmask_b32_e64 v7, 0, 1, vcc
	v_cmp_eq_u32_e32 vcc, v9, v0
	s_nop 1
	v_addc_co_u32_e32 v10, vcc, v6, v7, vcc
	ds_read_b128 v[6:9], v67 offset:42160
	s_waitcnt lgkmcnt(1)
	v_cmp_eq_u32_e32 vcc, v2, v0
	s_nop 1
	v_cndmask_b32_e64 v2, 0, 1, vcc
	v_cmp_eq_u32_e32 vcc, v3, v0
	s_nop 1
	v_addc_co_u32_e32 v2, vcc, v10, v2, vcc
	v_cmp_eq_u32_e32 vcc, v4, v0
	s_nop 1
	v_cndmask_b32_e64 v3, 0, 1, vcc
	v_cmp_eq_u32_e32 vcc, v5, v0
	s_nop 1
	v_addc_co_u32_e32 v2, vcc, v2, v3, vcc
	s_waitcnt lgkmcnt(0)
	v_cmp_eq_u32_e32 vcc, v6, v0
	s_nop 1
	v_cndmask_b32_e64 v3, 0, 1, vcc
	v_cmp_eq_u32_e32 vcc, v7, v0
	s_nop 1
	v_addc_co_u32_e32 v6, vcc, v2, v3, vcc
	ds_read_b128 v[2:5], v67 offset:42176
	v_cmp_eq_u32_e32 vcc, v8, v0
	s_nop 1
	v_cndmask_b32_e64 v7, 0, 1, vcc
	v_cmp_eq_u32_e32 vcc, v9, v0
	s_nop 1
	v_addc_co_u32_e32 v10, vcc, v6, v7, vcc
	ds_read_b128 v[6:9], v67 offset:42192
	s_waitcnt lgkmcnt(1)
	v_cmp_eq_u32_e32 vcc, v2, v0
	s_nop 1
	v_cndmask_b32_e64 v2, 0, 1, vcc
	v_cmp_eq_u32_e32 vcc, v3, v0
	s_nop 1
	v_addc_co_u32_e32 v2, vcc, v10, v2, vcc
	v_cmp_eq_u32_e32 vcc, v4, v0
	s_nop 1
	v_cndmask_b32_e64 v3, 0, 1, vcc
	v_cmp_eq_u32_e32 vcc, v5, v0
	s_nop 1
	v_addc_co_u32_e32 v2, vcc, v2, v3, vcc
	s_waitcnt lgkmcnt(0)
	v_cmp_eq_u32_e32 vcc, v6, v0
	s_nop 1
	v_cndmask_b32_e64 v3, 0, 1, vcc
	v_cmp_eq_u32_e32 vcc, v7, v0
	s_nop 1
	v_addc_co_u32_e32 v6, vcc, v2, v3, vcc
	ds_read_b128 v[2:5], v67 offset:42208
	v_cmp_eq_u32_e32 vcc, v8, v0
	s_nop 1
	v_cndmask_b32_e64 v7, 0, 1, vcc
	v_cmp_eq_u32_e32 vcc, v9, v0
	s_nop 1
	v_addc_co_u32_e32 v10, vcc, v6, v7, vcc
	ds_read_b128 v[6:9], v67 offset:42224
	s_waitcnt lgkmcnt(1)
	v_cmp_eq_u32_e32 vcc, v2, v0
	s_nop 1
	v_cndmask_b32_e64 v2, 0, 1, vcc
	v_cmp_eq_u32_e32 vcc, v3, v0
	s_nop 1
	v_addc_co_u32_e32 v2, vcc, v10, v2, vcc
	v_cmp_eq_u32_e32 vcc, v4, v0
	s_nop 1
	v_cndmask_b32_e64 v3, 0, 1, vcc
	v_cmp_eq_u32_e32 vcc, v5, v0
	s_nop 1
	v_addc_co_u32_e32 v2, vcc, v2, v3, vcc
	s_waitcnt lgkmcnt(0)
	v_cmp_eq_u32_e32 vcc, v6, v0
	s_nop 1
	v_cndmask_b32_e64 v3, 0, 1, vcc
	v_cmp_eq_u32_e32 vcc, v7, v0
	s_nop 1
	v_addc_co_u32_e32 v6, vcc, v2, v3, vcc
	ds_read_b128 v[2:5], v67 offset:42240
	v_cmp_eq_u32_e32 vcc, v8, v0
	s_nop 1
	v_cndmask_b32_e64 v7, 0, 1, vcc
	v_cmp_eq_u32_e32 vcc, v9, v0
	s_nop 1
	v_addc_co_u32_e32 v10, vcc, v6, v7, vcc
	ds_read_b128 v[6:9], v67 offset:42256
	s_waitcnt lgkmcnt(1)
	v_cmp_eq_u32_e32 vcc, v2, v0
	s_nop 1
	v_cndmask_b32_e64 v2, 0, 1, vcc
	v_cmp_eq_u32_e32 vcc, v3, v0
	s_nop 1
	v_addc_co_u32_e32 v2, vcc, v10, v2, vcc
	v_cmp_eq_u32_e32 vcc, v4, v0
	s_nop 1
	v_cndmask_b32_e64 v3, 0, 1, vcc
	v_cmp_eq_u32_e32 vcc, v5, v0
	s_nop 1
	v_addc_co_u32_e32 v2, vcc, v2, v3, vcc
	s_waitcnt lgkmcnt(0)
	v_cmp_eq_u32_e32 vcc, v6, v0
	s_nop 1
	v_cndmask_b32_e64 v3, 0, 1, vcc
	v_cmp_eq_u32_e32 vcc, v7, v0
	s_nop 1
	v_addc_co_u32_e32 v6, vcc, v2, v3, vcc
	ds_read_b128 v[2:5], v67 offset:42272
	v_cmp_eq_u32_e32 vcc, v8, v0
	s_nop 1
	v_cndmask_b32_e64 v7, 0, 1, vcc
	v_cmp_eq_u32_e32 vcc, v9, v0
	s_nop 1
	v_addc_co_u32_e32 v10, vcc, v6, v7, vcc
	ds_read_b128 v[6:9], v67 offset:42288
	s_waitcnt lgkmcnt(1)
	v_cmp_eq_u32_e32 vcc, v2, v0
	s_nop 1
	v_cndmask_b32_e64 v2, 0, 1, vcc
	v_cmp_eq_u32_e32 vcc, v3, v0
	s_nop 1
	v_addc_co_u32_e32 v2, vcc, v10, v2, vcc
	v_cmp_eq_u32_e32 vcc, v4, v0
	s_nop 1
	v_cndmask_b32_e64 v3, 0, 1, vcc
	v_cmp_eq_u32_e32 vcc, v5, v0
	s_nop 1
	v_addc_co_u32_e32 v2, vcc, v2, v3, vcc
	s_waitcnt lgkmcnt(0)
	v_cmp_eq_u32_e32 vcc, v6, v0
	s_nop 1
	v_cndmask_b32_e64 v3, 0, 1, vcc
	v_cmp_eq_u32_e32 vcc, v7, v0
	s_nop 1
	v_addc_co_u32_e32 v6, vcc, v2, v3, vcc
	ds_read_b128 v[2:5], v67 offset:42304
	v_cmp_eq_u32_e32 vcc, v8, v0
	s_nop 1
	v_cndmask_b32_e64 v7, 0, 1, vcc
	v_cmp_eq_u32_e32 vcc, v9, v0
	s_nop 1
	v_addc_co_u32_e32 v10, vcc, v6, v7, vcc
	ds_read_b128 v[6:9], v67 offset:42320
	s_waitcnt lgkmcnt(1)
	v_cmp_eq_u32_e32 vcc, v2, v0
	s_nop 1
	v_cndmask_b32_e64 v2, 0, 1, vcc
	v_cmp_eq_u32_e32 vcc, v3, v0
	s_nop 1
	v_addc_co_u32_e32 v2, vcc, v10, v2, vcc
	v_cmp_eq_u32_e32 vcc, v4, v0
	s_nop 1
	v_cndmask_b32_e64 v3, 0, 1, vcc
	v_cmp_eq_u32_e32 vcc, v5, v0
	s_nop 1
	v_addc_co_u32_e32 v2, vcc, v2, v3, vcc
	s_waitcnt lgkmcnt(0)
	v_cmp_eq_u32_e32 vcc, v6, v0
	s_nop 1
	v_cndmask_b32_e64 v3, 0, 1, vcc
	v_cmp_eq_u32_e32 vcc, v7, v0
	s_nop 1
	v_addc_co_u32_e32 v6, vcc, v2, v3, vcc
	ds_read_b128 v[2:5], v67 offset:42336
	v_cmp_eq_u32_e32 vcc, v8, v0
	s_nop 1
	v_cndmask_b32_e64 v7, 0, 1, vcc
	v_cmp_eq_u32_e32 vcc, v9, v0
	s_nop 1
	v_addc_co_u32_e32 v10, vcc, v6, v7, vcc
	ds_read_b128 v[6:9], v67 offset:42352
	s_waitcnt lgkmcnt(1)
	v_cmp_eq_u32_e32 vcc, v2, v0
	s_nop 1
	v_cndmask_b32_e64 v2, 0, 1, vcc
	v_cmp_eq_u32_e32 vcc, v3, v0
	s_nop 1
	v_addc_co_u32_e32 v2, vcc, v10, v2, vcc
	v_cmp_eq_u32_e32 vcc, v4, v0
	s_nop 1
	v_cndmask_b32_e64 v3, 0, 1, vcc
	v_cmp_eq_u32_e32 vcc, v5, v0
	s_nop 1
	v_addc_co_u32_e32 v2, vcc, v2, v3, vcc
	s_waitcnt lgkmcnt(0)
	v_cmp_eq_u32_e32 vcc, v6, v0
	s_nop 1
	v_cndmask_b32_e64 v3, 0, 1, vcc
	v_cmp_eq_u32_e32 vcc, v7, v0
	s_nop 1
	v_addc_co_u32_e32 v6, vcc, v2, v3, vcc
	ds_read_b128 v[2:5], v67 offset:42368
	v_cmp_eq_u32_e32 vcc, v8, v0
	s_nop 1
	v_cndmask_b32_e64 v7, 0, 1, vcc
	v_cmp_eq_u32_e32 vcc, v9, v0
	s_nop 1
	v_addc_co_u32_e32 v10, vcc, v6, v7, vcc
	ds_read_b128 v[6:9], v67 offset:42384
	s_waitcnt lgkmcnt(1)
	v_cmp_eq_u32_e32 vcc, v2, v0
	s_nop 1
	v_cndmask_b32_e64 v2, 0, 1, vcc
	v_cmp_eq_u32_e32 vcc, v3, v0
	s_nop 1
	v_addc_co_u32_e32 v2, vcc, v10, v2, vcc
	v_cmp_eq_u32_e32 vcc, v4, v0
	s_nop 1
	v_cndmask_b32_e64 v3, 0, 1, vcc
	v_cmp_eq_u32_e32 vcc, v5, v0
	s_nop 1
	v_addc_co_u32_e32 v2, vcc, v2, v3, vcc
	s_waitcnt lgkmcnt(0)
	v_cmp_eq_u32_e32 vcc, v6, v0
	s_nop 1
	v_cndmask_b32_e64 v3, 0, 1, vcc
	v_cmp_eq_u32_e32 vcc, v7, v0
	s_nop 1
	v_addc_co_u32_e32 v6, vcc, v2, v3, vcc
	ds_read_b128 v[2:5], v67 offset:42400
	v_cmp_eq_u32_e32 vcc, v8, v0
	s_nop 1
	v_cndmask_b32_e64 v7, 0, 1, vcc
	v_cmp_eq_u32_e32 vcc, v9, v0
	s_nop 1
	v_addc_co_u32_e32 v10, vcc, v6, v7, vcc
	ds_read_b128 v[6:9], v67 offset:42416
	s_waitcnt lgkmcnt(1)
	v_cmp_eq_u32_e32 vcc, v2, v0
	s_nop 1
	v_cndmask_b32_e64 v2, 0, 1, vcc
	v_cmp_eq_u32_e32 vcc, v3, v0
	s_nop 1
	v_addc_co_u32_e32 v2, vcc, v10, v2, vcc
	v_cmp_eq_u32_e32 vcc, v4, v0
	s_nop 1
	v_cndmask_b32_e64 v3, 0, 1, vcc
	v_cmp_eq_u32_e32 vcc, v5, v0
	s_nop 1
	v_addc_co_u32_e32 v2, vcc, v2, v3, vcc
	s_waitcnt lgkmcnt(0)
	v_cmp_eq_u32_e32 vcc, v6, v0
	s_nop 1
	v_cndmask_b32_e64 v3, 0, 1, vcc
	v_cmp_eq_u32_e32 vcc, v7, v0
	s_nop 1
	v_addc_co_u32_e32 v6, vcc, v2, v3, vcc
	ds_read_b128 v[2:5], v67 offset:42432
	v_cmp_eq_u32_e32 vcc, v8, v0
	s_nop 1
	v_cndmask_b32_e64 v7, 0, 1, vcc
	v_cmp_eq_u32_e32 vcc, v9, v0
	s_nop 1
	v_addc_co_u32_e32 v10, vcc, v6, v7, vcc
	ds_read_b128 v[6:9], v67 offset:42448
	s_waitcnt lgkmcnt(1)
	v_cmp_eq_u32_e32 vcc, v2, v0
	s_nop 1
	v_cndmask_b32_e64 v2, 0, 1, vcc
	v_cmp_eq_u32_e32 vcc, v3, v0
	s_nop 1
	v_addc_co_u32_e32 v2, vcc, v10, v2, vcc
	v_cmp_eq_u32_e32 vcc, v4, v0
	s_nop 1
	v_cndmask_b32_e64 v3, 0, 1, vcc
	v_cmp_eq_u32_e32 vcc, v5, v0
	s_nop 1
	v_addc_co_u32_e32 v2, vcc, v2, v3, vcc
	s_waitcnt lgkmcnt(0)
	v_cmp_eq_u32_e32 vcc, v6, v0
	s_nop 1
	v_cndmask_b32_e64 v3, 0, 1, vcc
	v_cmp_eq_u32_e32 vcc, v7, v0
	s_nop 1
	v_addc_co_u32_e32 v6, vcc, v2, v3, vcc
	ds_read_b128 v[2:5], v67 offset:42464
	v_cmp_eq_u32_e32 vcc, v8, v0
	s_nop 1
	v_cndmask_b32_e64 v7, 0, 1, vcc
	v_cmp_eq_u32_e32 vcc, v9, v0
	s_nop 1
	v_addc_co_u32_e32 v10, vcc, v6, v7, vcc
	ds_read_b128 v[6:9], v67 offset:42480
	s_waitcnt lgkmcnt(1)
	v_cmp_eq_u32_e32 vcc, v2, v0
	s_nop 1
	v_cndmask_b32_e64 v2, 0, 1, vcc
	v_cmp_eq_u32_e32 vcc, v3, v0
	s_nop 1
	v_addc_co_u32_e32 v2, vcc, v10, v2, vcc
	v_cmp_eq_u32_e32 vcc, v4, v0
	s_nop 1
	v_cndmask_b32_e64 v3, 0, 1, vcc
	v_cmp_eq_u32_e32 vcc, v5, v0
	s_nop 1
	v_addc_co_u32_e32 v2, vcc, v2, v3, vcc
	s_waitcnt lgkmcnt(0)
	v_cmp_eq_u32_e32 vcc, v6, v0
	s_nop 1
	v_cndmask_b32_e64 v3, 0, 1, vcc
	v_cmp_eq_u32_e32 vcc, v7, v0
	s_nop 1
	v_addc_co_u32_e32 v2, vcc, v2, v3, vcc
	v_cmp_eq_u32_e32 vcc, v8, v0
	s_nop 1
	v_cndmask_b32_e64 v3, 0, 1, vcc
	v_cmp_eq_u32_e32 vcc, v9, v0
	s_nop 1
	v_addc_co_u32_e32 v2, vcc, v2, v3, vcc
	v_cmp_ne_u32_e32 vcc, 0, v2
	s_and_b64 exec, exec, vcc
	s_cbranch_execz .LBB0_1283
	global_atomic_add v2, v[70:71], v2, off sc0
	s_mov_b32 s8, s88
	ds_read_b128 v[114:117], v67 offset:41984
	ds_read_b128 v[118:121], v67 offset:42000
	ds_read_b128 v[122:125], v67 offset:42016
	ds_read_b128 v[126:129], v67 offset:42032
	ds_read_b128 v[130:133], v67 offset:42048
	ds_read_b128 v[134:137], v67 offset:42064
	ds_read_b128 v[138:141], v67 offset:42080
	ds_read_b128 v[142:145], v67 offset:42096
	ds_read_b128 v[146:149], v67 offset:42112
	ds_read_b128 v[150:153], v67 offset:42128
	ds_read_b128 v[154:157], v67 offset:42144
	ds_read_b128 v[158:161], v67 offset:42160
	ds_read_b128 v[162:165], v67 offset:42176
	ds_read_b128 v[166:169], v67 offset:42192
	ds_read_b128 v[170:173], v67 offset:42208
	ds_read_b128 v[174:177], v67 offset:42224
	s_waitcnt vmcnt(0)
	s_waitcnt lgkmcnt(15)
	v_cmp_eq_u32_e32 vcc, v114, v0
	s_and_saveexec_b64 s[10:11], vcc
	s_cbranch_execz .Lp8s_0_0
	s_ashr_i32 s9, s8, 31
	v_ashrrev_i32_e32 v3, 31, v2
	s_lshl_b64 s[14:15], s[8:9], 4
	v_lshl_add_u64 v[4:5], v[2:3], 2, v[72:73]
	v_mov_b32_e32 v3, s8
	s_add_u32 s14, s86, s14
	global_store_dword v[4:5], v3, off
	v_add_u32_e32 v3, v2, v94
	s_addc_u32 s15, s87, s15
	v_add_u32_e32 v2, 1, v2
	global_store_dword v67, v3, s[14:15]
.Lp8s_0_0:
	s_or_b64 exec, exec, s[10:11]
	v_cmp_eq_u32_e32 vcc, v115, v0
	s_and_saveexec_b64 s[10:11], vcc
	s_cbranch_execz .Lp8s_0_1
	s_ashr_i32 s9, s8, 31
	v_ashrrev_i32_e32 v3, 31, v2
	s_lshl_b64 s[14:15], s[8:9], 4
	v_lshl_add_u64 v[4:5], v[2:3], 2, v[72:73]
	v_mov_b32_e32 v3, s8
	s_add_u32 s14, s86, s14
	global_store_dword v[4:5], v3, off
	v_add_u32_e32 v3, v2, v94
	s_addc_u32 s15, s87, s15
	v_add_u32_e32 v2, 1, v2
	global_store_dword v67, v3, s[14:15] offset:4
.Lp8s_0_1:
	s_or_b64 exec, exec, s[10:11]
	v_cmp_eq_u32_e32 vcc, v116, v0
	s_and_saveexec_b64 s[10:11], vcc
	s_cbranch_execz .Lp8s_0_2
	s_ashr_i32 s9, s8, 31
	v_ashrrev_i32_e32 v3, 31, v2
	s_lshl_b64 s[14:15], s[8:9], 4
	v_lshl_add_u64 v[4:5], v[2:3], 2, v[72:73]
	v_mov_b32_e32 v3, s8
	s_add_u32 s14, s86, s14
	global_store_dword v[4:5], v3, off
	v_add_u32_e32 v3, v2, v94
	s_addc_u32 s15, s87, s15
	v_add_u32_e32 v2, 1, v2
	global_store_dword v67, v3, s[14:15] offset:8
.Lp8s_0_2:
	s_or_b64 exec, exec, s[10:11]
	v_cmp_eq_u32_e32 vcc, v117, v0
	s_and_saveexec_b64 s[10:11], vcc
	s_cbranch_execz .Lp8s_0_3
	s_ashr_i32 s9, s8, 31
	v_ashrrev_i32_e32 v3, 31, v2
	s_lshl_b64 s[14:15], s[8:9], 4
	v_lshl_add_u64 v[4:5], v[2:3], 2, v[72:73]
	v_mov_b32_e32 v3, s8
	s_add_u32 s14, s86, s14
	global_store_dword v[4:5], v3, off
	v_add_u32_e32 v3, v2, v94
	s_addc_u32 s15, s87, s15
	v_add_u32_e32 v2, 1, v2
	global_store_dword v67, v3, s[14:15] offset:12
.Lp8s_0_3:
	s_or_b64 exec, exec, s[10:11]
	s_add_i32 s8, s8, 1
	s_waitcnt lgkmcnt(14)
	v_cmp_eq_u32_e32 vcc, v118, v0
	s_and_saveexec_b64 s[10:11], vcc
	s_cbranch_execz .Lp8s_1_0
	s_ashr_i32 s9, s8, 31
	v_ashrrev_i32_e32 v3, 31, v2
	s_lshl_b64 s[14:15], s[8:9], 4
	v_lshl_add_u64 v[4:5], v[2:3], 2, v[72:73]
	v_mov_b32_e32 v3, s8
	s_add_u32 s14, s86, s14
	global_store_dword v[4:5], v3, off
	v_add_u32_e32 v3, v2, v94
	s_addc_u32 s15, s87, s15
	v_add_u32_e32 v2, 1, v2
	global_store_dword v67, v3, s[14:15]
.Lp8s_1_0:
	s_or_b64 exec, exec, s[10:11]
	v_cmp_eq_u32_e32 vcc, v119, v0
	s_and_saveexec_b64 s[10:11], vcc
	s_cbranch_execz .Lp8s_1_1
	s_ashr_i32 s9, s8, 31
	v_ashrrev_i32_e32 v3, 31, v2
	s_lshl_b64 s[14:15], s[8:9], 4
	v_lshl_add_u64 v[4:5], v[2:3], 2, v[72:73]
	v_mov_b32_e32 v3, s8
	s_add_u32 s14, s86, s14
	global_store_dword v[4:5], v3, off
	v_add_u32_e32 v3, v2, v94
	s_addc_u32 s15, s87, s15
	v_add_u32_e32 v2, 1, v2
	global_store_dword v67, v3, s[14:15] offset:4
.Lp8s_1_1:
	s_or_b64 exec, exec, s[10:11]
	v_cmp_eq_u32_e32 vcc, v120, v0
	s_and_saveexec_b64 s[10:11], vcc
	s_cbranch_execz .Lp8s_1_2
	s_ashr_i32 s9, s8, 31
	v_ashrrev_i32_e32 v3, 31, v2
	s_lshl_b64 s[14:15], s[8:9], 4
	v_lshl_add_u64 v[4:5], v[2:3], 2, v[72:73]
	v_mov_b32_e32 v3, s8
	s_add_u32 s14, s86, s14
	global_store_dword v[4:5], v3, off
	v_add_u32_e32 v3, v2, v94
	s_addc_u32 s15, s87, s15
	v_add_u32_e32 v2, 1, v2
	global_store_dword v67, v3, s[14:15] offset:8
.Lp8s_1_2:
	s_or_b64 exec, exec, s[10:11]
	v_cmp_eq_u32_e32 vcc, v121, v0
	s_and_saveexec_b64 s[10:11], vcc
	s_cbranch_execz .Lp8s_1_3
	s_ashr_i32 s9, s8, 31
	v_ashrrev_i32_e32 v3, 31, v2
	s_lshl_b64 s[14:15], s[8:9], 4
	v_lshl_add_u64 v[4:5], v[2:3], 2, v[72:73]
	v_mov_b32_e32 v3, s8
	s_add_u32 s14, s86, s14
	global_store_dword v[4:5], v3, off
	v_add_u32_e32 v3, v2, v94
	s_addc_u32 s15, s87, s15
	v_add_u32_e32 v2, 1, v2
	global_store_dword v67, v3, s[14:15] offset:12
.Lp8s_1_3:
	s_or_b64 exec, exec, s[10:11]
	s_add_i32 s8, s8, 1
	s_waitcnt lgkmcnt(13)
	v_cmp_eq_u32_e32 vcc, v122, v0
	s_and_saveexec_b64 s[10:11], vcc
	s_cbranch_execz .Lp8s_2_0
	s_ashr_i32 s9, s8, 31
	v_ashrrev_i32_e32 v3, 31, v2
	s_lshl_b64 s[14:15], s[8:9], 4
	v_lshl_add_u64 v[4:5], v[2:3], 2, v[72:73]
	v_mov_b32_e32 v3, s8
	s_add_u32 s14, s86, s14
	global_store_dword v[4:5], v3, off
	v_add_u32_e32 v3, v2, v94
	s_addc_u32 s15, s87, s15
	v_add_u32_e32 v2, 1, v2
	global_store_dword v67, v3, s[14:15]
.Lp8s_2_0:
	s_or_b64 exec, exec, s[10:11]
	v_cmp_eq_u32_e32 vcc, v123, v0
	s_and_saveexec_b64 s[10:11], vcc
	s_cbranch_execz .Lp8s_2_1
	s_ashr_i32 s9, s8, 31
	v_ashrrev_i32_e32 v3, 31, v2
	s_lshl_b64 s[14:15], s[8:9], 4
	v_lshl_add_u64 v[4:5], v[2:3], 2, v[72:73]
	v_mov_b32_e32 v3, s8
	s_add_u32 s14, s86, s14
	global_store_dword v[4:5], v3, off
	v_add_u32_e32 v3, v2, v94
	s_addc_u32 s15, s87, s15
	v_add_u32_e32 v2, 1, v2
	global_store_dword v67, v3, s[14:15] offset:4
.Lp8s_2_1:
	s_or_b64 exec, exec, s[10:11]
	v_cmp_eq_u32_e32 vcc, v124, v0
	s_and_saveexec_b64 s[10:11], vcc
	s_cbranch_execz .Lp8s_2_2
	s_ashr_i32 s9, s8, 31
	v_ashrrev_i32_e32 v3, 31, v2
	s_lshl_b64 s[14:15], s[8:9], 4
	v_lshl_add_u64 v[4:5], v[2:3], 2, v[72:73]
	v_mov_b32_e32 v3, s8
	s_add_u32 s14, s86, s14
	global_store_dword v[4:5], v3, off
	v_add_u32_e32 v3, v2, v94
	s_addc_u32 s15, s87, s15
	v_add_u32_e32 v2, 1, v2
	global_store_dword v67, v3, s[14:15] offset:8
.Lp8s_2_2:
	s_or_b64 exec, exec, s[10:11]
	v_cmp_eq_u32_e32 vcc, v125, v0
	s_and_saveexec_b64 s[10:11], vcc
	s_cbranch_execz .Lp8s_2_3
	s_ashr_i32 s9, s8, 31
	v_ashrrev_i32_e32 v3, 31, v2
	s_lshl_b64 s[14:15], s[8:9], 4
	v_lshl_add_u64 v[4:5], v[2:3], 2, v[72:73]
	v_mov_b32_e32 v3, s8
	s_add_u32 s14, s86, s14
	global_store_dword v[4:5], v3, off
	v_add_u32_e32 v3, v2, v94
	s_addc_u32 s15, s87, s15
	v_add_u32_e32 v2, 1, v2
	global_store_dword v67, v3, s[14:15] offset:12
.Lp8s_2_3:
	s_or_b64 exec, exec, s[10:11]
	s_add_i32 s8, s8, 1
	s_waitcnt lgkmcnt(12)
	v_cmp_eq_u32_e32 vcc, v126, v0
	s_and_saveexec_b64 s[10:11], vcc
	s_cbranch_execz .Lp8s_3_0
	s_ashr_i32 s9, s8, 31
	v_ashrrev_i32_e32 v3, 31, v2
	s_lshl_b64 s[14:15], s[8:9], 4
	v_lshl_add_u64 v[4:5], v[2:3], 2, v[72:73]
	v_mov_b32_e32 v3, s8
	s_add_u32 s14, s86, s14
	global_store_dword v[4:5], v3, off
	v_add_u32_e32 v3, v2, v94
	s_addc_u32 s15, s87, s15
	v_add_u32_e32 v2, 1, v2
	global_store_dword v67, v3, s[14:15]
.Lp8s_3_0:
	s_or_b64 exec, exec, s[10:11]
	v_cmp_eq_u32_e32 vcc, v127, v0
	s_and_saveexec_b64 s[10:11], vcc
	s_cbranch_execz .Lp8s_3_1
	s_ashr_i32 s9, s8, 31
	v_ashrrev_i32_e32 v3, 31, v2
	s_lshl_b64 s[14:15], s[8:9], 4
	v_lshl_add_u64 v[4:5], v[2:3], 2, v[72:73]
	v_mov_b32_e32 v3, s8
	s_add_u32 s14, s86, s14
	global_store_dword v[4:5], v3, off
	v_add_u32_e32 v3, v2, v94
	s_addc_u32 s15, s87, s15
	v_add_u32_e32 v2, 1, v2
	global_store_dword v67, v3, s[14:15] offset:4
.Lp8s_3_1:
	s_or_b64 exec, exec, s[10:11]
	v_cmp_eq_u32_e32 vcc, v128, v0
	s_and_saveexec_b64 s[10:11], vcc
	s_cbranch_execz .Lp8s_3_2
	s_ashr_i32 s9, s8, 31
	v_ashrrev_i32_e32 v3, 31, v2
	s_lshl_b64 s[14:15], s[8:9], 4
	v_lshl_add_u64 v[4:5], v[2:3], 2, v[72:73]
	v_mov_b32_e32 v3, s8
	s_add_u32 s14, s86, s14
	global_store_dword v[4:5], v3, off
	v_add_u32_e32 v3, v2, v94
	s_addc_u32 s15, s87, s15
	v_add_u32_e32 v2, 1, v2
	global_store_dword v67, v3, s[14:15] offset:8
.Lp8s_3_2:
	s_or_b64 exec, exec, s[10:11]
	v_cmp_eq_u32_e32 vcc, v129, v0
	s_and_saveexec_b64 s[10:11], vcc
	s_cbranch_execz .Lp8s_3_3
	s_ashr_i32 s9, s8, 31
	v_ashrrev_i32_e32 v3, 31, v2
	s_lshl_b64 s[14:15], s[8:9], 4
	v_lshl_add_u64 v[4:5], v[2:3], 2, v[72:73]
	v_mov_b32_e32 v3, s8
	s_add_u32 s14, s86, s14
	global_store_dword v[4:5], v3, off
	v_add_u32_e32 v3, v2, v94
	s_addc_u32 s15, s87, s15
	v_add_u32_e32 v2, 1, v2
	global_store_dword v67, v3, s[14:15] offset:12
.Lp8s_3_3:
	s_or_b64 exec, exec, s[10:11]
	s_add_i32 s8, s8, 1
	s_waitcnt lgkmcnt(11)
	v_cmp_eq_u32_e32 vcc, v130, v0
	s_and_saveexec_b64 s[10:11], vcc
	s_cbranch_execz .Lp8s_4_0
	s_ashr_i32 s9, s8, 31
	v_ashrrev_i32_e32 v3, 31, v2
	s_lshl_b64 s[14:15], s[8:9], 4
	v_lshl_add_u64 v[4:5], v[2:3], 2, v[72:73]
	v_mov_b32_e32 v3, s8
	s_add_u32 s14, s86, s14
	global_store_dword v[4:5], v3, off
	v_add_u32_e32 v3, v2, v94
	s_addc_u32 s15, s87, s15
	v_add_u32_e32 v2, 1, v2
	global_store_dword v67, v3, s[14:15]
.Lp8s_4_0:
	s_or_b64 exec, exec, s[10:11]
	v_cmp_eq_u32_e32 vcc, v131, v0
	s_and_saveexec_b64 s[10:11], vcc
	s_cbranch_execz .Lp8s_4_1
	s_ashr_i32 s9, s8, 31
	v_ashrrev_i32_e32 v3, 31, v2
	s_lshl_b64 s[14:15], s[8:9], 4
	v_lshl_add_u64 v[4:5], v[2:3], 2, v[72:73]
	v_mov_b32_e32 v3, s8
	s_add_u32 s14, s86, s14
	global_store_dword v[4:5], v3, off
	v_add_u32_e32 v3, v2, v94
	s_addc_u32 s15, s87, s15
	v_add_u32_e32 v2, 1, v2
	global_store_dword v67, v3, s[14:15] offset:4
.Lp8s_4_1:
	s_or_b64 exec, exec, s[10:11]
	v_cmp_eq_u32_e32 vcc, v132, v0
	s_and_saveexec_b64 s[10:11], vcc
	s_cbranch_execz .Lp8s_4_2
	s_ashr_i32 s9, s8, 31
	v_ashrrev_i32_e32 v3, 31, v2
	s_lshl_b64 s[14:15], s[8:9], 4
	v_lshl_add_u64 v[4:5], v[2:3], 2, v[72:73]
	v_mov_b32_e32 v3, s8
	s_add_u32 s14, s86, s14
	global_store_dword v[4:5], v3, off
	v_add_u32_e32 v3, v2, v94
	s_addc_u32 s15, s87, s15
	v_add_u32_e32 v2, 1, v2
	global_store_dword v67, v3, s[14:15] offset:8
.Lp8s_4_2:
	s_or_b64 exec, exec, s[10:11]
	v_cmp_eq_u32_e32 vcc, v133, v0
	s_and_saveexec_b64 s[10:11], vcc
	s_cbranch_execz .Lp8s_4_3
	s_ashr_i32 s9, s8, 31
	v_ashrrev_i32_e32 v3, 31, v2
	s_lshl_b64 s[14:15], s[8:9], 4
	v_lshl_add_u64 v[4:5], v[2:3], 2, v[72:73]
	v_mov_b32_e32 v3, s8
	s_add_u32 s14, s86, s14
	global_store_dword v[4:5], v3, off
	v_add_u32_e32 v3, v2, v94
	s_addc_u32 s15, s87, s15
	v_add_u32_e32 v2, 1, v2
	global_store_dword v67, v3, s[14:15] offset:12
.Lp8s_4_3:
	s_or_b64 exec, exec, s[10:11]
	s_add_i32 s8, s8, 1
	s_waitcnt lgkmcnt(10)
	v_cmp_eq_u32_e32 vcc, v134, v0
	s_and_saveexec_b64 s[10:11], vcc
	s_cbranch_execz .Lp8s_5_0
	s_ashr_i32 s9, s8, 31
	v_ashrrev_i32_e32 v3, 31, v2
	s_lshl_b64 s[14:15], s[8:9], 4
	v_lshl_add_u64 v[4:5], v[2:3], 2, v[72:73]
	v_mov_b32_e32 v3, s8
	s_add_u32 s14, s86, s14
	global_store_dword v[4:5], v3, off
	v_add_u32_e32 v3, v2, v94
	s_addc_u32 s15, s87, s15
	v_add_u32_e32 v2, 1, v2
	global_store_dword v67, v3, s[14:15]
.Lp8s_5_0:
	s_or_b64 exec, exec, s[10:11]
	v_cmp_eq_u32_e32 vcc, v135, v0
	s_and_saveexec_b64 s[10:11], vcc
	s_cbranch_execz .Lp8s_5_1
	s_ashr_i32 s9, s8, 31
	v_ashrrev_i32_e32 v3, 31, v2
	s_lshl_b64 s[14:15], s[8:9], 4
	v_lshl_add_u64 v[4:5], v[2:3], 2, v[72:73]
	v_mov_b32_e32 v3, s8
	s_add_u32 s14, s86, s14
	global_store_dword v[4:5], v3, off
	v_add_u32_e32 v3, v2, v94
	s_addc_u32 s15, s87, s15
	v_add_u32_e32 v2, 1, v2
	global_store_dword v67, v3, s[14:15] offset:4
.Lp8s_5_1:
	s_or_b64 exec, exec, s[10:11]
	v_cmp_eq_u32_e32 vcc, v136, v0
	s_and_saveexec_b64 s[10:11], vcc
	s_cbranch_execz .Lp8s_5_2
	s_ashr_i32 s9, s8, 31
	v_ashrrev_i32_e32 v3, 31, v2
	s_lshl_b64 s[14:15], s[8:9], 4
	v_lshl_add_u64 v[4:5], v[2:3], 2, v[72:73]
	v_mov_b32_e32 v3, s8
	s_add_u32 s14, s86, s14
	global_store_dword v[4:5], v3, off
	v_add_u32_e32 v3, v2, v94
	s_addc_u32 s15, s87, s15
	v_add_u32_e32 v2, 1, v2
	global_store_dword v67, v3, s[14:15] offset:8
.Lp8s_5_2:
	s_or_b64 exec, exec, s[10:11]
	v_cmp_eq_u32_e32 vcc, v137, v0
	s_and_saveexec_b64 s[10:11], vcc
	s_cbranch_execz .Lp8s_5_3
	s_ashr_i32 s9, s8, 31
	v_ashrrev_i32_e32 v3, 31, v2
	s_lshl_b64 s[14:15], s[8:9], 4
	v_lshl_add_u64 v[4:5], v[2:3], 2, v[72:73]
	v_mov_b32_e32 v3, s8
	s_add_u32 s14, s86, s14
	global_store_dword v[4:5], v3, off
	v_add_u32_e32 v3, v2, v94
	s_addc_u32 s15, s87, s15
	v_add_u32_e32 v2, 1, v2
	global_store_dword v67, v3, s[14:15] offset:12
.Lp8s_5_3:
	s_or_b64 exec, exec, s[10:11]
	s_add_i32 s8, s8, 1
	s_waitcnt lgkmcnt(9)
	v_cmp_eq_u32_e32 vcc, v138, v0
	s_and_saveexec_b64 s[10:11], vcc
	s_cbranch_execz .Lp8s_6_0
	s_ashr_i32 s9, s8, 31
	v_ashrrev_i32_e32 v3, 31, v2
	s_lshl_b64 s[14:15], s[8:9], 4
	v_lshl_add_u64 v[4:5], v[2:3], 2, v[72:73]
	v_mov_b32_e32 v3, s8
	s_add_u32 s14, s86, s14
	global_store_dword v[4:5], v3, off
	v_add_u32_e32 v3, v2, v94
	s_addc_u32 s15, s87, s15
	v_add_u32_e32 v2, 1, v2
	global_store_dword v67, v3, s[14:15]
.Lp8s_6_0:
	s_or_b64 exec, exec, s[10:11]
	v_cmp_eq_u32_e32 vcc, v139, v0
	s_and_saveexec_b64 s[10:11], vcc
	s_cbranch_execz .Lp8s_6_1
	s_ashr_i32 s9, s8, 31
	v_ashrrev_i32_e32 v3, 31, v2
	s_lshl_b64 s[14:15], s[8:9], 4
	v_lshl_add_u64 v[4:5], v[2:3], 2, v[72:73]
	v_mov_b32_e32 v3, s8
	s_add_u32 s14, s86, s14
	global_store_dword v[4:5], v3, off
	v_add_u32_e32 v3, v2, v94
	s_addc_u32 s15, s87, s15
	v_add_u32_e32 v2, 1, v2
	global_store_dword v67, v3, s[14:15] offset:4
.Lp8s_6_1:
	s_or_b64 exec, exec, s[10:11]
	v_cmp_eq_u32_e32 vcc, v140, v0
	s_and_saveexec_b64 s[10:11], vcc
	s_cbranch_execz .Lp8s_6_2
	s_ashr_i32 s9, s8, 31
	v_ashrrev_i32_e32 v3, 31, v2
	s_lshl_b64 s[14:15], s[8:9], 4
	v_lshl_add_u64 v[4:5], v[2:3], 2, v[72:73]
	v_mov_b32_e32 v3, s8
	s_add_u32 s14, s86, s14
	global_store_dword v[4:5], v3, off
	v_add_u32_e32 v3, v2, v94
	s_addc_u32 s15, s87, s15
	v_add_u32_e32 v2, 1, v2
	global_store_dword v67, v3, s[14:15] offset:8
.Lp8s_6_2:
	s_or_b64 exec, exec, s[10:11]
	v_cmp_eq_u32_e32 vcc, v141, v0
	s_and_saveexec_b64 s[10:11], vcc
	s_cbranch_execz .Lp8s_6_3
	s_ashr_i32 s9, s8, 31
	v_ashrrev_i32_e32 v3, 31, v2
	s_lshl_b64 s[14:15], s[8:9], 4
	v_lshl_add_u64 v[4:5], v[2:3], 2, v[72:73]
	v_mov_b32_e32 v3, s8
	s_add_u32 s14, s86, s14
	global_store_dword v[4:5], v3, off
	v_add_u32_e32 v3, v2, v94
	s_addc_u32 s15, s87, s15
	v_add_u32_e32 v2, 1, v2
	global_store_dword v67, v3, s[14:15] offset:12
.Lp8s_6_3:
	s_or_b64 exec, exec, s[10:11]
	s_add_i32 s8, s8, 1
	s_waitcnt lgkmcnt(8)
	v_cmp_eq_u32_e32 vcc, v142, v0
	s_and_saveexec_b64 s[10:11], vcc
	s_cbranch_execz .Lp8s_7_0
	s_ashr_i32 s9, s8, 31
	v_ashrrev_i32_e32 v3, 31, v2
	s_lshl_b64 s[14:15], s[8:9], 4
	v_lshl_add_u64 v[4:5], v[2:3], 2, v[72:73]
	v_mov_b32_e32 v3, s8
	s_add_u32 s14, s86, s14
	global_store_dword v[4:5], v3, off
	v_add_u32_e32 v3, v2, v94
	s_addc_u32 s15, s87, s15
	v_add_u32_e32 v2, 1, v2
	global_store_dword v67, v3, s[14:15]
.Lp8s_7_0:
	s_or_b64 exec, exec, s[10:11]
	v_cmp_eq_u32_e32 vcc, v143, v0
	s_and_saveexec_b64 s[10:11], vcc
	s_cbranch_execz .Lp8s_7_1
	s_ashr_i32 s9, s8, 31
	v_ashrrev_i32_e32 v3, 31, v2
	s_lshl_b64 s[14:15], s[8:9], 4
	v_lshl_add_u64 v[4:5], v[2:3], 2, v[72:73]
	v_mov_b32_e32 v3, s8
	s_add_u32 s14, s86, s14
	global_store_dword v[4:5], v3, off
	v_add_u32_e32 v3, v2, v94
	s_addc_u32 s15, s87, s15
	v_add_u32_e32 v2, 1, v2
	global_store_dword v67, v3, s[14:15] offset:4
.Lp8s_7_1:
	s_or_b64 exec, exec, s[10:11]
	v_cmp_eq_u32_e32 vcc, v144, v0
	s_and_saveexec_b64 s[10:11], vcc
	s_cbranch_execz .Lp8s_7_2
	s_ashr_i32 s9, s8, 31
	v_ashrrev_i32_e32 v3, 31, v2
	s_lshl_b64 s[14:15], s[8:9], 4
	v_lshl_add_u64 v[4:5], v[2:3], 2, v[72:73]
	v_mov_b32_e32 v3, s8
	s_add_u32 s14, s86, s14
	global_store_dword v[4:5], v3, off
	v_add_u32_e32 v3, v2, v94
	s_addc_u32 s15, s87, s15
	v_add_u32_e32 v2, 1, v2
	global_store_dword v67, v3, s[14:15] offset:8
.Lp8s_7_2:
	s_or_b64 exec, exec, s[10:11]
	v_cmp_eq_u32_e32 vcc, v145, v0
	s_and_saveexec_b64 s[10:11], vcc
	s_cbranch_execz .Lp8s_7_3
	s_ashr_i32 s9, s8, 31
	v_ashrrev_i32_e32 v3, 31, v2
	s_lshl_b64 s[14:15], s[8:9], 4
	v_lshl_add_u64 v[4:5], v[2:3], 2, v[72:73]
	v_mov_b32_e32 v3, s8
	s_add_u32 s14, s86, s14
	global_store_dword v[4:5], v3, off
	v_add_u32_e32 v3, v2, v94
	s_addc_u32 s15, s87, s15
	v_add_u32_e32 v2, 1, v2
	global_store_dword v67, v3, s[14:15] offset:12
.Lp8s_7_3:
	s_or_b64 exec, exec, s[10:11]
	s_add_i32 s8, s8, 1
	s_waitcnt lgkmcnt(7)
	v_cmp_eq_u32_e32 vcc, v146, v0
	s_and_saveexec_b64 s[10:11], vcc
	s_cbranch_execz .Lp8s_8_0
	s_ashr_i32 s9, s8, 31
	v_ashrrev_i32_e32 v3, 31, v2
	s_lshl_b64 s[14:15], s[8:9], 4
	v_lshl_add_u64 v[4:5], v[2:3], 2, v[72:73]
	v_mov_b32_e32 v3, s8
	s_add_u32 s14, s86, s14
	global_store_dword v[4:5], v3, off
	v_add_u32_e32 v3, v2, v94
	s_addc_u32 s15, s87, s15
	v_add_u32_e32 v2, 1, v2
	global_store_dword v67, v3, s[14:15]
.Lp8s_8_0:
	s_or_b64 exec, exec, s[10:11]
	v_cmp_eq_u32_e32 vcc, v147, v0
	s_and_saveexec_b64 s[10:11], vcc
	s_cbranch_execz .Lp8s_8_1
	s_ashr_i32 s9, s8, 31
	v_ashrrev_i32_e32 v3, 31, v2
	s_lshl_b64 s[14:15], s[8:9], 4
	v_lshl_add_u64 v[4:5], v[2:3], 2, v[72:73]
	v_mov_b32_e32 v3, s8
	s_add_u32 s14, s86, s14
	global_store_dword v[4:5], v3, off
	v_add_u32_e32 v3, v2, v94
	s_addc_u32 s15, s87, s15
	v_add_u32_e32 v2, 1, v2
	global_store_dword v67, v3, s[14:15] offset:4
.Lp8s_8_1:
	s_or_b64 exec, exec, s[10:11]
	v_cmp_eq_u32_e32 vcc, v148, v0
	s_and_saveexec_b64 s[10:11], vcc
	s_cbranch_execz .Lp8s_8_2
	s_ashr_i32 s9, s8, 31
	v_ashrrev_i32_e32 v3, 31, v2
	s_lshl_b64 s[14:15], s[8:9], 4
	v_lshl_add_u64 v[4:5], v[2:3], 2, v[72:73]
	v_mov_b32_e32 v3, s8
	s_add_u32 s14, s86, s14
	global_store_dword v[4:5], v3, off
	v_add_u32_e32 v3, v2, v94
	s_addc_u32 s15, s87, s15
	v_add_u32_e32 v2, 1, v2
	global_store_dword v67, v3, s[14:15] offset:8
.Lp8s_8_2:
	s_or_b64 exec, exec, s[10:11]
	v_cmp_eq_u32_e32 vcc, v149, v0
	s_and_saveexec_b64 s[10:11], vcc
	s_cbranch_execz .Lp8s_8_3
	s_ashr_i32 s9, s8, 31
	v_ashrrev_i32_e32 v3, 31, v2
	s_lshl_b64 s[14:15], s[8:9], 4
	v_lshl_add_u64 v[4:5], v[2:3], 2, v[72:73]
	v_mov_b32_e32 v3, s8
	s_add_u32 s14, s86, s14
	global_store_dword v[4:5], v3, off
	v_add_u32_e32 v3, v2, v94
	s_addc_u32 s15, s87, s15
	v_add_u32_e32 v2, 1, v2
	global_store_dword v67, v3, s[14:15] offset:12
.Lp8s_8_3:
	s_or_b64 exec, exec, s[10:11]
	s_add_i32 s8, s8, 1
	s_waitcnt lgkmcnt(6)
	v_cmp_eq_u32_e32 vcc, v150, v0
	s_and_saveexec_b64 s[10:11], vcc
	s_cbranch_execz .Lp8s_9_0
	s_ashr_i32 s9, s8, 31
	v_ashrrev_i32_e32 v3, 31, v2
	s_lshl_b64 s[14:15], s[8:9], 4
	v_lshl_add_u64 v[4:5], v[2:3], 2, v[72:73]
	v_mov_b32_e32 v3, s8
	s_add_u32 s14, s86, s14
	global_store_dword v[4:5], v3, off
	v_add_u32_e32 v3, v2, v94
	s_addc_u32 s15, s87, s15
	v_add_u32_e32 v2, 1, v2
	global_store_dword v67, v3, s[14:15]
.Lp8s_9_0:
	s_or_b64 exec, exec, s[10:11]
	v_cmp_eq_u32_e32 vcc, v151, v0
	s_and_saveexec_b64 s[10:11], vcc
	s_cbranch_execz .Lp8s_9_1
	s_ashr_i32 s9, s8, 31
	v_ashrrev_i32_e32 v3, 31, v2
	s_lshl_b64 s[14:15], s[8:9], 4
	v_lshl_add_u64 v[4:5], v[2:3], 2, v[72:73]
	v_mov_b32_e32 v3, s8
	s_add_u32 s14, s86, s14
	global_store_dword v[4:5], v3, off
	v_add_u32_e32 v3, v2, v94
	s_addc_u32 s15, s87, s15
	v_add_u32_e32 v2, 1, v2
	global_store_dword v67, v3, s[14:15] offset:4
.Lp8s_9_1:
	s_or_b64 exec, exec, s[10:11]
	v_cmp_eq_u32_e32 vcc, v152, v0
	s_and_saveexec_b64 s[10:11], vcc
	s_cbranch_execz .Lp8s_9_2
	s_ashr_i32 s9, s8, 31
	v_ashrrev_i32_e32 v3, 31, v2
	s_lshl_b64 s[14:15], s[8:9], 4
	v_lshl_add_u64 v[4:5], v[2:3], 2, v[72:73]
	v_mov_b32_e32 v3, s8
	s_add_u32 s14, s86, s14
	global_store_dword v[4:5], v3, off
	v_add_u32_e32 v3, v2, v94
	s_addc_u32 s15, s87, s15
	v_add_u32_e32 v2, 1, v2
	global_store_dword v67, v3, s[14:15] offset:8
.Lp8s_9_2:
	s_or_b64 exec, exec, s[10:11]
	v_cmp_eq_u32_e32 vcc, v153, v0
	s_and_saveexec_b64 s[10:11], vcc
	s_cbranch_execz .Lp8s_9_3
	s_ashr_i32 s9, s8, 31
	v_ashrrev_i32_e32 v3, 31, v2
	s_lshl_b64 s[14:15], s[8:9], 4
	v_lshl_add_u64 v[4:5], v[2:3], 2, v[72:73]
	v_mov_b32_e32 v3, s8
	s_add_u32 s14, s86, s14
	global_store_dword v[4:5], v3, off
	v_add_u32_e32 v3, v2, v94
	s_addc_u32 s15, s87, s15
	v_add_u32_e32 v2, 1, v2
	global_store_dword v67, v3, s[14:15] offset:12
.Lp8s_9_3:
	s_or_b64 exec, exec, s[10:11]
	s_add_i32 s8, s8, 1
	s_waitcnt lgkmcnt(5)
	v_cmp_eq_u32_e32 vcc, v154, v0
	s_and_saveexec_b64 s[10:11], vcc
	s_cbranch_execz .Lp8s_10_0
	s_ashr_i32 s9, s8, 31
	v_ashrrev_i32_e32 v3, 31, v2
	s_lshl_b64 s[14:15], s[8:9], 4
	v_lshl_add_u64 v[4:5], v[2:3], 2, v[72:73]
	v_mov_b32_e32 v3, s8
	s_add_u32 s14, s86, s14
	global_store_dword v[4:5], v3, off
	v_add_u32_e32 v3, v2, v94
	s_addc_u32 s15, s87, s15
	v_add_u32_e32 v2, 1, v2
	global_store_dword v67, v3, s[14:15]
.Lp8s_10_0:
	s_or_b64 exec, exec, s[10:11]
	v_cmp_eq_u32_e32 vcc, v155, v0
	s_and_saveexec_b64 s[10:11], vcc
	s_cbranch_execz .Lp8s_10_1
	s_ashr_i32 s9, s8, 31
	v_ashrrev_i32_e32 v3, 31, v2
	s_lshl_b64 s[14:15], s[8:9], 4
	v_lshl_add_u64 v[4:5], v[2:3], 2, v[72:73]
	v_mov_b32_e32 v3, s8
	s_add_u32 s14, s86, s14
	global_store_dword v[4:5], v3, off
	v_add_u32_e32 v3, v2, v94
	s_addc_u32 s15, s87, s15
	v_add_u32_e32 v2, 1, v2
	global_store_dword v67, v3, s[14:15] offset:4
.Lp8s_10_1:
	s_or_b64 exec, exec, s[10:11]
	v_cmp_eq_u32_e32 vcc, v156, v0
	s_and_saveexec_b64 s[10:11], vcc
	s_cbranch_execz .Lp8s_10_2
	s_ashr_i32 s9, s8, 31
	v_ashrrev_i32_e32 v3, 31, v2
	s_lshl_b64 s[14:15], s[8:9], 4
	v_lshl_add_u64 v[4:5], v[2:3], 2, v[72:73]
	v_mov_b32_e32 v3, s8
	s_add_u32 s14, s86, s14
	global_store_dword v[4:5], v3, off
	v_add_u32_e32 v3, v2, v94
	s_addc_u32 s15, s87, s15
	v_add_u32_e32 v2, 1, v2
	global_store_dword v67, v3, s[14:15] offset:8
.Lp8s_10_2:
	s_or_b64 exec, exec, s[10:11]
	v_cmp_eq_u32_e32 vcc, v157, v0
	s_and_saveexec_b64 s[10:11], vcc
	s_cbranch_execz .Lp8s_10_3
	s_ashr_i32 s9, s8, 31
	v_ashrrev_i32_e32 v3, 31, v2
	s_lshl_b64 s[14:15], s[8:9], 4
	v_lshl_add_u64 v[4:5], v[2:3], 2, v[72:73]
	v_mov_b32_e32 v3, s8
	s_add_u32 s14, s86, s14
	global_store_dword v[4:5], v3, off
	v_add_u32_e32 v3, v2, v94
	s_addc_u32 s15, s87, s15
	v_add_u32_e32 v2, 1, v2
	global_store_dword v67, v3, s[14:15] offset:12
.Lp8s_10_3:
	s_or_b64 exec, exec, s[10:11]
	s_add_i32 s8, s8, 1
	s_waitcnt lgkmcnt(4)
	v_cmp_eq_u32_e32 vcc, v158, v0
	s_and_saveexec_b64 s[10:11], vcc
	s_cbranch_execz .Lp8s_11_0
	s_ashr_i32 s9, s8, 31
	v_ashrrev_i32_e32 v3, 31, v2
	s_lshl_b64 s[14:15], s[8:9], 4
	v_lshl_add_u64 v[4:5], v[2:3], 2, v[72:73]
	v_mov_b32_e32 v3, s8
	s_add_u32 s14, s86, s14
	global_store_dword v[4:5], v3, off
	v_add_u32_e32 v3, v2, v94
	s_addc_u32 s15, s87, s15
	v_add_u32_e32 v2, 1, v2
	global_store_dword v67, v3, s[14:15]
.Lp8s_11_0:
	s_or_b64 exec, exec, s[10:11]
	v_cmp_eq_u32_e32 vcc, v159, v0
	s_and_saveexec_b64 s[10:11], vcc
	s_cbranch_execz .Lp8s_11_1
	s_ashr_i32 s9, s8, 31
	v_ashrrev_i32_e32 v3, 31, v2
	s_lshl_b64 s[14:15], s[8:9], 4
	v_lshl_add_u64 v[4:5], v[2:3], 2, v[72:73]
	v_mov_b32_e32 v3, s8
	s_add_u32 s14, s86, s14
	global_store_dword v[4:5], v3, off
	v_add_u32_e32 v3, v2, v94
	s_addc_u32 s15, s87, s15
	v_add_u32_e32 v2, 1, v2
	global_store_dword v67, v3, s[14:15] offset:4
.Lp8s_11_1:
	s_or_b64 exec, exec, s[10:11]
	v_cmp_eq_u32_e32 vcc, v160, v0
	s_and_saveexec_b64 s[10:11], vcc
	s_cbranch_execz .Lp8s_11_2
	s_ashr_i32 s9, s8, 31
	v_ashrrev_i32_e32 v3, 31, v2
	s_lshl_b64 s[14:15], s[8:9], 4
	v_lshl_add_u64 v[4:5], v[2:3], 2, v[72:73]
	v_mov_b32_e32 v3, s8
	s_add_u32 s14, s86, s14
	global_store_dword v[4:5], v3, off
	v_add_u32_e32 v3, v2, v94
	s_addc_u32 s15, s87, s15
	v_add_u32_e32 v2, 1, v2
	global_store_dword v67, v3, s[14:15] offset:8
.Lp8s_11_2:
	s_or_b64 exec, exec, s[10:11]
	v_cmp_eq_u32_e32 vcc, v161, v0
	s_and_saveexec_b64 s[10:11], vcc
	s_cbranch_execz .Lp8s_11_3
	s_ashr_i32 s9, s8, 31
	v_ashrrev_i32_e32 v3, 31, v2
	s_lshl_b64 s[14:15], s[8:9], 4
	v_lshl_add_u64 v[4:5], v[2:3], 2, v[72:73]
	v_mov_b32_e32 v3, s8
	s_add_u32 s14, s86, s14
	global_store_dword v[4:5], v3, off
	v_add_u32_e32 v3, v2, v94
	s_addc_u32 s15, s87, s15
	v_add_u32_e32 v2, 1, v2
	global_store_dword v67, v3, s[14:15] offset:12
.Lp8s_11_3:
	s_or_b64 exec, exec, s[10:11]
	s_add_i32 s8, s8, 1
	s_waitcnt lgkmcnt(3)
	v_cmp_eq_u32_e32 vcc, v162, v0
	s_and_saveexec_b64 s[10:11], vcc
	s_cbranch_execz .Lp8s_12_0
	s_ashr_i32 s9, s8, 31
	v_ashrrev_i32_e32 v3, 31, v2
	s_lshl_b64 s[14:15], s[8:9], 4
	v_lshl_add_u64 v[4:5], v[2:3], 2, v[72:73]
	v_mov_b32_e32 v3, s8
	s_add_u32 s14, s86, s14
	global_store_dword v[4:5], v3, off
	v_add_u32_e32 v3, v2, v94
	s_addc_u32 s15, s87, s15
	v_add_u32_e32 v2, 1, v2
	global_store_dword v67, v3, s[14:15]
.Lp8s_12_0:
	s_or_b64 exec, exec, s[10:11]
	v_cmp_eq_u32_e32 vcc, v163, v0
	s_and_saveexec_b64 s[10:11], vcc
	s_cbranch_execz .Lp8s_12_1
	s_ashr_i32 s9, s8, 31
	v_ashrrev_i32_e32 v3, 31, v2
	s_lshl_b64 s[14:15], s[8:9], 4
	v_lshl_add_u64 v[4:5], v[2:3], 2, v[72:73]
	v_mov_b32_e32 v3, s8
	s_add_u32 s14, s86, s14
	global_store_dword v[4:5], v3, off
	v_add_u32_e32 v3, v2, v94
	s_addc_u32 s15, s87, s15
	v_add_u32_e32 v2, 1, v2
	global_store_dword v67, v3, s[14:15] offset:4
.Lp8s_12_1:
	s_or_b64 exec, exec, s[10:11]
	v_cmp_eq_u32_e32 vcc, v164, v0
	s_and_saveexec_b64 s[10:11], vcc
	s_cbranch_execz .Lp8s_12_2
	s_ashr_i32 s9, s8, 31
	v_ashrrev_i32_e32 v3, 31, v2
	s_lshl_b64 s[14:15], s[8:9], 4
	v_lshl_add_u64 v[4:5], v[2:3], 2, v[72:73]
	v_mov_b32_e32 v3, s8
	s_add_u32 s14, s86, s14
	global_store_dword v[4:5], v3, off
	v_add_u32_e32 v3, v2, v94
	s_addc_u32 s15, s87, s15
	v_add_u32_e32 v2, 1, v2
	global_store_dword v67, v3, s[14:15] offset:8
.Lp8s_12_2:
	s_or_b64 exec, exec, s[10:11]
	v_cmp_eq_u32_e32 vcc, v165, v0
	s_and_saveexec_b64 s[10:11], vcc
	s_cbranch_execz .Lp8s_12_3
	s_ashr_i32 s9, s8, 31
	v_ashrrev_i32_e32 v3, 31, v2
	s_lshl_b64 s[14:15], s[8:9], 4
	v_lshl_add_u64 v[4:5], v[2:3], 2, v[72:73]
	v_mov_b32_e32 v3, s8
	s_add_u32 s14, s86, s14
	global_store_dword v[4:5], v3, off
	v_add_u32_e32 v3, v2, v94
	s_addc_u32 s15, s87, s15
	v_add_u32_e32 v2, 1, v2
	global_store_dword v67, v3, s[14:15] offset:12
.Lp8s_12_3:
	s_or_b64 exec, exec, s[10:11]
	s_add_i32 s8, s8, 1
	s_waitcnt lgkmcnt(2)
	v_cmp_eq_u32_e32 vcc, v166, v0
	s_and_saveexec_b64 s[10:11], vcc
	s_cbranch_execz .Lp8s_13_0
	s_ashr_i32 s9, s8, 31
	v_ashrrev_i32_e32 v3, 31, v2
	s_lshl_b64 s[14:15], s[8:9], 4
	v_lshl_add_u64 v[4:5], v[2:3], 2, v[72:73]
	v_mov_b32_e32 v3, s8
	s_add_u32 s14, s86, s14
	global_store_dword v[4:5], v3, off
	v_add_u32_e32 v3, v2, v94
	s_addc_u32 s15, s87, s15
	v_add_u32_e32 v2, 1, v2
	global_store_dword v67, v3, s[14:15]
.Lp8s_13_0:
	s_or_b64 exec, exec, s[10:11]
	v_cmp_eq_u32_e32 vcc, v167, v0
	s_and_saveexec_b64 s[10:11], vcc
	s_cbranch_execz .Lp8s_13_1
	s_ashr_i32 s9, s8, 31
	v_ashrrev_i32_e32 v3, 31, v2
	s_lshl_b64 s[14:15], s[8:9], 4
	v_lshl_add_u64 v[4:5], v[2:3], 2, v[72:73]
	v_mov_b32_e32 v3, s8
	s_add_u32 s14, s86, s14
	global_store_dword v[4:5], v3, off
	v_add_u32_e32 v3, v2, v94
	s_addc_u32 s15, s87, s15
	v_add_u32_e32 v2, 1, v2
	global_store_dword v67, v3, s[14:15] offset:4
.Lp8s_13_1:
	s_or_b64 exec, exec, s[10:11]
	v_cmp_eq_u32_e32 vcc, v168, v0
	s_and_saveexec_b64 s[10:11], vcc
	s_cbranch_execz .Lp8s_13_2
	s_ashr_i32 s9, s8, 31
	v_ashrrev_i32_e32 v3, 31, v2
	s_lshl_b64 s[14:15], s[8:9], 4
	v_lshl_add_u64 v[4:5], v[2:3], 2, v[72:73]
	v_mov_b32_e32 v3, s8
	s_add_u32 s14, s86, s14
	global_store_dword v[4:5], v3, off
	v_add_u32_e32 v3, v2, v94
	s_addc_u32 s15, s87, s15
	v_add_u32_e32 v2, 1, v2
	global_store_dword v67, v3, s[14:15] offset:8
.Lp8s_13_2:
	s_or_b64 exec, exec, s[10:11]
	v_cmp_eq_u32_e32 vcc, v169, v0
	s_and_saveexec_b64 s[10:11], vcc
	s_cbranch_execz .Lp8s_13_3
	s_ashr_i32 s9, s8, 31
	v_ashrrev_i32_e32 v3, 31, v2
	s_lshl_b64 s[14:15], s[8:9], 4
	v_lshl_add_u64 v[4:5], v[2:3], 2, v[72:73]
	v_mov_b32_e32 v3, s8
	s_add_u32 s14, s86, s14
	global_store_dword v[4:5], v3, off
	v_add_u32_e32 v3, v2, v94
	s_addc_u32 s15, s87, s15
	v_add_u32_e32 v2, 1, v2
	global_store_dword v67, v3, s[14:15] offset:12
.Lp8s_13_3:
	s_or_b64 exec, exec, s[10:11]
	s_add_i32 s8, s8, 1
	s_waitcnt lgkmcnt(1)
	v_cmp_eq_u32_e32 vcc, v170, v0
	s_and_saveexec_b64 s[10:11], vcc
	s_cbranch_execz .Lp8s_14_0
	s_ashr_i32 s9, s8, 31
	v_ashrrev_i32_e32 v3, 31, v2
	s_lshl_b64 s[14:15], s[8:9], 4
	v_lshl_add_u64 v[4:5], v[2:3], 2, v[72:73]
	v_mov_b32_e32 v3, s8
	s_add_u32 s14, s86, s14
	global_store_dword v[4:5], v3, off
	v_add_u32_e32 v3, v2, v94
	s_addc_u32 s15, s87, s15
	v_add_u32_e32 v2, 1, v2
	global_store_dword v67, v3, s[14:15]
.Lp8s_14_0:
	s_or_b64 exec, exec, s[10:11]
	v_cmp_eq_u32_e32 vcc, v171, v0
	s_and_saveexec_b64 s[10:11], vcc
	s_cbranch_execz .Lp8s_14_1
	s_ashr_i32 s9, s8, 31
	v_ashrrev_i32_e32 v3, 31, v2
	s_lshl_b64 s[14:15], s[8:9], 4
	v_lshl_add_u64 v[4:5], v[2:3], 2, v[72:73]
	v_mov_b32_e32 v3, s8
	s_add_u32 s14, s86, s14
	global_store_dword v[4:5], v3, off
	v_add_u32_e32 v3, v2, v94
	s_addc_u32 s15, s87, s15
	v_add_u32_e32 v2, 1, v2
	global_store_dword v67, v3, s[14:15] offset:4
.Lp8s_14_1:
	s_or_b64 exec, exec, s[10:11]
	v_cmp_eq_u32_e32 vcc, v172, v0
	s_and_saveexec_b64 s[10:11], vcc
	s_cbranch_execz .Lp8s_14_2
	s_ashr_i32 s9, s8, 31
	v_ashrrev_i32_e32 v3, 31, v2
	s_lshl_b64 s[14:15], s[8:9], 4
	v_lshl_add_u64 v[4:5], v[2:3], 2, v[72:73]
	v_mov_b32_e32 v3, s8
	s_add_u32 s14, s86, s14
	global_store_dword v[4:5], v3, off
	v_add_u32_e32 v3, v2, v94
	s_addc_u32 s15, s87, s15
	v_add_u32_e32 v2, 1, v2
	global_store_dword v67, v3, s[14:15] offset:8
.Lp8s_14_2:
	s_or_b64 exec, exec, s[10:11]
	v_cmp_eq_u32_e32 vcc, v173, v0
	s_and_saveexec_b64 s[10:11], vcc
	s_cbranch_execz .Lp8s_14_3
	s_ashr_i32 s9, s8, 31
	v_ashrrev_i32_e32 v3, 31, v2
	s_lshl_b64 s[14:15], s[8:9], 4
	v_lshl_add_u64 v[4:5], v[2:3], 2, v[72:73]
	v_mov_b32_e32 v3, s8
	s_add_u32 s14, s86, s14
	global_store_dword v[4:5], v3, off
	v_add_u32_e32 v3, v2, v94
	s_addc_u32 s15, s87, s15
	v_add_u32_e32 v2, 1, v2
	global_store_dword v67, v3, s[14:15] offset:12
.Lp8s_14_3:
	s_or_b64 exec, exec, s[10:11]
	s_add_i32 s8, s8, 1
	s_waitcnt lgkmcnt(0)
	v_cmp_eq_u32_e32 vcc, v174, v0
	s_and_saveexec_b64 s[10:11], vcc
	s_cbranch_execz .Lp8s_15_0
	s_ashr_i32 s9, s8, 31
	v_ashrrev_i32_e32 v3, 31, v2
	s_lshl_b64 s[14:15], s[8:9], 4
	v_lshl_add_u64 v[4:5], v[2:3], 2, v[72:73]
	v_mov_b32_e32 v3, s8
	s_add_u32 s14, s86, s14
	global_store_dword v[4:5], v3, off
	v_add_u32_e32 v3, v2, v94
	s_addc_u32 s15, s87, s15
	v_add_u32_e32 v2, 1, v2
	global_store_dword v67, v3, s[14:15]
.Lp8s_15_0:
	s_or_b64 exec, exec, s[10:11]
	v_cmp_eq_u32_e32 vcc, v175, v0
	s_and_saveexec_b64 s[10:11], vcc
	s_cbranch_execz .Lp8s_15_1
	s_ashr_i32 s9, s8, 31
	v_ashrrev_i32_e32 v3, 31, v2
	s_lshl_b64 s[14:15], s[8:9], 4
	v_lshl_add_u64 v[4:5], v[2:3], 2, v[72:73]
	v_mov_b32_e32 v3, s8
	s_add_u32 s14, s86, s14
	global_store_dword v[4:5], v3, off
	v_add_u32_e32 v3, v2, v94
	s_addc_u32 s15, s87, s15
	v_add_u32_e32 v2, 1, v2
	global_store_dword v67, v3, s[14:15] offset:4
.Lp8s_15_1:
	s_or_b64 exec, exec, s[10:11]
	v_cmp_eq_u32_e32 vcc, v176, v0
	s_and_saveexec_b64 s[10:11], vcc
	s_cbranch_execz .Lp8s_15_2
	s_ashr_i32 s9, s8, 31
	v_ashrrev_i32_e32 v3, 31, v2
	s_lshl_b64 s[14:15], s[8:9], 4
	v_lshl_add_u64 v[4:5], v[2:3], 2, v[72:73]
	v_mov_b32_e32 v3, s8
	s_add_u32 s14, s86, s14
	global_store_dword v[4:5], v3, off
	v_add_u32_e32 v3, v2, v94
	s_addc_u32 s15, s87, s15
	v_add_u32_e32 v2, 1, v2
	global_store_dword v67, v3, s[14:15] offset:8
.Lp8s_15_2:
	s_or_b64 exec, exec, s[10:11]
	v_cmp_eq_u32_e32 vcc, v177, v0
	s_and_saveexec_b64 s[10:11], vcc
	s_cbranch_execz .Lp8s_15_3
	s_ashr_i32 s9, s8, 31
	v_ashrrev_i32_e32 v3, 31, v2
	s_lshl_b64 s[14:15], s[8:9], 4
	v_lshl_add_u64 v[4:5], v[2:3], 2, v[72:73]
	v_mov_b32_e32 v3, s8
	s_add_u32 s14, s86, s14
	global_store_dword v[4:5], v3, off
	v_add_u32_e32 v3, v2, v94
	s_addc_u32 s15, s87, s15
	v_add_u32_e32 v2, 1, v2
	global_store_dword v67, v3, s[14:15] offset:12
.Lp8s_15_3:
	s_or_b64 exec, exec, s[10:11]
	s_add_i32 s8, s8, 1
	ds_read_b128 v[114:117], v67 offset:42240
	ds_read_b128 v[118:121], v67 offset:42256
	ds_read_b128 v[122:125], v67 offset:42272
	ds_read_b128 v[126:129], v67 offset:42288
	ds_read_b128 v[130:133], v67 offset:42304
	ds_read_b128 v[134:137], v67 offset:42320
	ds_read_b128 v[138:141], v67 offset:42336
	ds_read_b128 v[142:145], v67 offset:42352
	ds_read_b128 v[146:149], v67 offset:42368
	ds_read_b128 v[150:153], v67 offset:42384
	ds_read_b128 v[154:157], v67 offset:42400
	ds_read_b128 v[158:161], v67 offset:42416
	ds_read_b128 v[162:165], v67 offset:42432
	ds_read_b128 v[166:169], v67 offset:42448
	ds_read_b128 v[170:173], v67 offset:42464
	ds_read_b128 v[174:177], v67 offset:42480
	s_waitcnt lgkmcnt(15)
	v_cmp_eq_u32_e32 vcc, v114, v0
	s_and_saveexec_b64 s[10:11], vcc
	s_cbranch_execz .Lp8s_16_0
	s_ashr_i32 s9, s8, 31
	v_ashrrev_i32_e32 v3, 31, v2
	s_lshl_b64 s[14:15], s[8:9], 4
	v_lshl_add_u64 v[4:5], v[2:3], 2, v[72:73]
	v_mov_b32_e32 v3, s8
	s_add_u32 s14, s86, s14
	global_store_dword v[4:5], v3, off
	v_add_u32_e32 v3, v2, v94
	s_addc_u32 s15, s87, s15
	v_add_u32_e32 v2, 1, v2
	global_store_dword v67, v3, s[14:15]

.Lp8s_31_3:
	s_or_b64 exec, exec, s[10:11]
	s_add_i32 s8, s8, 1
	s_branch .LBB0_1283
